# baseline (speedup 1.0000x reference)
.Lw_ld_done:
	s_waitcnt vmcnt(60)
	v_and_b32_e32 v242, 0xffff0000, v3
	v_lshlrev_b32_e32 v240, 3, v0
	v_sub_f32_e32 v244, v3, v242
	v_and_b32_e32 v242, 0xffff0000, v4
	v_and_b32_e32 v148, 0xf8, v240
	v_and_b32_e32 v240, 0xffff0000, v2
	v_sub_f32_e32 v245, v4, v242
	v_and_b32_e32 v242, 0xffff0000, v5
	v_sub_f32_e32 v240, v2, v240
	v_sub_f32_e32 v246, v5, v242
	v_mad_u32_u24 v247, v1, s17, v148
	v_perm_b32 v242, v3, v2, s14
	v_perm_b32 v243, v5, v4, s14
	ds_write_b64 v247, v[242:243]
	v_perm_b32 v242, v244, v240, s14
	v_perm_b32 v243, v246, v245, s14
	ds_write_b64 v247, v[242:243] offset:13056
	v_and_b32_e32 v242, 0xffff0000, v7
	v_sub_f32_e32 v244, v7, v242
	v_and_b32_e32 v242, 0xffff0000, v8
	v_and_b32_e32 v240, 0xffff0000, v6
	v_sub_f32_e32 v245, v8, v242
	v_and_b32_e32 v242, 0xffff0000, v9
	v_sub_f32_e32 v240, v6, v240
	v_sub_f32_e32 v246, v9, v242
	v_mad_u32_u24 v241, v146, s17, v148
	v_perm_b32 v242, v7, v6, s14
	v_perm_b32 v243, v9, v8, s14
	ds_write_b64 v241, v[242:243]
	v_perm_b32 v242, v244, v240, s14
	v_perm_b32 v243, v246, v245, s14
	ds_write_b64 v241, v[242:243] offset:13056
	v_and_b32_e32 v242, 0xffff0000, v11
	v_sub_f32_e32 v244, v11, v242
	v_and_b32_e32 v242, 0xffff0000, v12
	v_and_b32_e32 v240, 0xffff0000, v10
	v_sub_f32_e32 v245, v12, v242
	v_and_b32_e32 v242, 0xffff0000, v13
	v_sub_f32_e32 v240, v10, v240
	v_sub_f32_e32 v246, v13, v242
	v_perm_b32 v242, v11, v10, s14
	v_perm_b32 v243, v13, v12, s14
	ds_write_b64 v247, v[242:243] offset:8704
	v_perm_b32 v242, v244, v240, s14
	v_perm_b32 v243, v246, v245, s14
	ds_write_b64 v247, v[242:243] offset:21760
	s_waitcnt lgkmcnt(0)
	s_barrier
	s_waitcnt vmcnt(0)
	v_cvt_pk_bf16_f32 v106, v112, v113
	v_lshlrev_b32_e32 v248, 16, v106
	v_and_b32_e32 v249, 0xffff0000, v106
	v_sub_f32_e32 v248, v112, v248
	v_sub_f32_e32 v249, v113, v249
	v_cvt_pk_bf16_f32 v102, v248, v249
	v_cvt_pk_bf16_f32 v107, v114, v115
	v_lshlrev_b32_e32 v250, 16, v107
	v_and_b32_e32 v251, 0xffff0000, v107
	v_sub_f32_e32 v250, v114, v250
	v_sub_f32_e32 v251, v115, v251
	v_cvt_pk_bf16_f32 v103, v250, v251
	v_cvt_pk_bf16_f32 v108, v116, v117
	v_lshlrev_b32_e32 v248, 16, v108
	v_and_b32_e32 v249, 0xffff0000, v108
	v_sub_f32_e32 v248, v116, v248
	v_sub_f32_e32 v249, v117, v249
	v_cvt_pk_bf16_f32 v104, v248, v249
	v_cvt_pk_bf16_f32 v109, v118, v119
	v_lshlrev_b32_e32 v250, 16, v109
	v_and_b32_e32 v251, 0xffff0000, v109
	v_sub_f32_e32 v250, v118, v250
	v_sub_f32_e32 v251, v119, v251
	v_cvt_pk_bf16_f32 v105, v250, v251
	v_cvt_pk_bf16_f32 v74, v176, v178
	v_lshlrev_b32_e32 v248, 16, v74
	v_and_b32_e32 v249, 0xffff0000, v74
	v_sub_f32_e32 v248, v176, v248
	v_sub_f32_e32 v249, v178, v249
	v_cvt_pk_bf16_f32 v70, v248, v249
	v_cvt_pk_bf16_f32 v75, v180, v182
	v_lshlrev_b32_e32 v250, 16, v75
	v_and_b32_e32 v251, 0xffff0000, v75
	v_sub_f32_e32 v250, v180, v250
	v_sub_f32_e32 v251, v182, v251
	v_cvt_pk_bf16_f32 v71, v250, v251
	v_cvt_pk_bf16_f32 v76, v184, v186
	v_lshlrev_b32_e32 v248, 16, v76
	v_and_b32_e32 v249, 0xffff0000, v76
	v_sub_f32_e32 v248, v184, v248
	v_sub_f32_e32 v249, v186, v249
	v_cvt_pk_bf16_f32 v72, v248, v249
	v_cvt_pk_bf16_f32 v77, v188, v190
	v_lshlrev_b32_e32 v250, 16, v77
	v_and_b32_e32 v251, 0xffff0000, v77
	v_sub_f32_e32 v250, v188, v250
	v_sub_f32_e32 v251, v190, v251
	v_cvt_pk_bf16_f32 v73, v250, v251
	v_cvt_pk_bf16_f32 v38, v177, v179
	v_lshlrev_b32_e32 v248, 16, v38
	v_and_b32_e32 v249, 0xffff0000, v38
	v_sub_f32_e32 v248, v177, v248
	v_sub_f32_e32 v249, v179, v249
	v_cvt_pk_bf16_f32 v42, v248, v249
	v_cvt_pk_bf16_f32 v39, v181, v183
	v_lshlrev_b32_e32 v250, 16, v39
	v_and_b32_e32 v251, 0xffff0000, v39
	v_sub_f32_e32 v250, v181, v250
	v_sub_f32_e32 v251, v183, v251
	v_cvt_pk_bf16_f32 v43, v250, v251
	v_cvt_pk_bf16_f32 v40, v185, v187
	v_lshlrev_b32_e32 v248, 16, v40
	v_and_b32_e32 v249, 0xffff0000, v40
	v_sub_f32_e32 v248, v185, v248
	v_sub_f32_e32 v249, v187, v249
	v_cvt_pk_bf16_f32 v44, v248, v249
	v_cvt_pk_bf16_f32 v41, v189, v191
	v_lshlrev_b32_e32 v250, 16, v41
	v_and_b32_e32 v251, 0xffff0000, v41
	v_sub_f32_e32 v250, v189, v250
	v_sub_f32_e32 v251, v191, v251
	v_cvt_pk_bf16_f32 v45, v250, v251
	v_cvt_pk_bf16_f32 v98, v120, v121
	v_lshlrev_b32_e32 v248, 16, v98
	v_and_b32_e32 v249, 0xffff0000, v98
	v_sub_f32_e32 v248, v120, v248
	v_sub_f32_e32 v249, v121, v249
	v_cvt_pk_bf16_f32 v94, v248, v249
	v_cvt_pk_bf16_f32 v99, v122, v123
	v_lshlrev_b32_e32 v250, 16, v99
	v_and_b32_e32 v251, 0xffff0000, v99
	v_sub_f32_e32 v250, v122, v250
	v_sub_f32_e32 v251, v123, v251
	v_cvt_pk_bf16_f32 v95, v250, v251
	v_cvt_pk_bf16_f32 v100, v124, v125
	v_lshlrev_b32_e32 v248, 16, v100
	v_and_b32_e32 v249, 0xffff0000, v100
	v_sub_f32_e32 v248, v124, v248
	v_sub_f32_e32 v249, v125, v249
	v_cvt_pk_bf16_f32 v96, v248, v249
	v_cvt_pk_bf16_f32 v101, v126, v127
	v_lshlrev_b32_e32 v250, 16, v101
	v_and_b32_e32 v251, 0xffff0000, v101
	v_sub_f32_e32 v250, v126, v250
	v_sub_f32_e32 v251, v127, v251
	v_cvt_pk_bf16_f32 v97, v250, v251
	v_cvt_pk_bf16_f32 v62, v192, v194
	v_lshlrev_b32_e32 v248, 16, v62
	v_and_b32_e32 v249, 0xffff0000, v62
	v_sub_f32_e32 v248, v192, v248
	v_sub_f32_e32 v249, v194, v249
	v_cvt_pk_bf16_f32 v66, v248, v249
	v_cvt_pk_bf16_f32 v63, v196, v198
	v_lshlrev_b32_e32 v250, 16, v63
	v_and_b32_e32 v251, 0xffff0000, v63
	v_sub_f32_e32 v250, v196, v250
	v_sub_f32_e32 v251, v198, v251
	v_cvt_pk_bf16_f32 v67, v250, v251
	v_cvt_pk_bf16_f32 v64, v200, v202
	v_lshlrev_b32_e32 v248, 16, v64
	v_and_b32_e32 v249, 0xffff0000, v64
	v_sub_f32_e32 v248, v200, v248
	v_sub_f32_e32 v249, v202, v249
	v_cvt_pk_bf16_f32 v68, v248, v249
	v_cvt_pk_bf16_f32 v65, v204, v206
	v_lshlrev_b32_e32 v250, 16, v65
	v_and_b32_e32 v251, 0xffff0000, v65
	v_sub_f32_e32 v250, v204, v250
	v_sub_f32_e32 v251, v206, v251
	v_cvt_pk_bf16_f32 v69, v250, v251
	v_cvt_pk_bf16_f32 v30, v193, v195
	v_lshlrev_b32_e32 v248, 16, v30
	v_and_b32_e32 v249, 0xffff0000, v30
	v_sub_f32_e32 v248, v193, v248
	v_sub_f32_e32 v249, v195, v249
	v_cvt_pk_bf16_f32 v34, v248, v249
	v_cvt_pk_bf16_f32 v31, v197, v199
	v_lshlrev_b32_e32 v250, 16, v31
	v_and_b32_e32 v251, 0xffff0000, v31
	v_sub_f32_e32 v250, v197, v250
	v_sub_f32_e32 v251, v199, v251
	v_cvt_pk_bf16_f32 v35, v250, v251
	v_cvt_pk_bf16_f32 v32, v201, v203
	v_lshlrev_b32_e32 v248, 16, v32
	v_and_b32_e32 v249, 0xffff0000, v32
	v_sub_f32_e32 v248, v201, v248
	v_sub_f32_e32 v249, v203, v249
	v_cvt_pk_bf16_f32 v36, v248, v249
	v_cvt_pk_bf16_f32 v33, v205, v207
	v_lshlrev_b32_e32 v250, 16, v33
	v_and_b32_e32 v251, 0xffff0000, v33
	v_sub_f32_e32 v250, v205, v250
	v_sub_f32_e32 v251, v207, v251
	v_cvt_pk_bf16_f32 v37, v250, v251
	v_cvt_pk_bf16_f32 v90, v128, v129
	v_lshlrev_b32_e32 v248, 16, v90
	v_and_b32_e32 v249, 0xffff0000, v90
	v_sub_f32_e32 v248, v128, v248
	v_sub_f32_e32 v249, v129, v249
	v_cvt_pk_bf16_f32 v86, v248, v249
	v_cvt_pk_bf16_f32 v91, v130, v131
	v_lshlrev_b32_e32 v250, 16, v91
	v_and_b32_e32 v251, 0xffff0000, v91
	v_sub_f32_e32 v250, v130, v250
	v_sub_f32_e32 v251, v131, v251
	v_cvt_pk_bf16_f32 v87, v250, v251
	v_cvt_pk_bf16_f32 v92, v132, v133
	v_lshlrev_b32_e32 v248, 16, v92
	v_and_b32_e32 v249, 0xffff0000, v92
	v_sub_f32_e32 v248, v132, v248
	v_sub_f32_e32 v249, v133, v249
	v_cvt_pk_bf16_f32 v88, v248, v249
	v_cvt_pk_bf16_f32 v93, v134, v135
	v_lshlrev_b32_e32 v250, 16, v93
	v_and_b32_e32 v251, 0xffff0000, v93
	v_sub_f32_e32 v250, v134, v250
	v_sub_f32_e32 v251, v135, v251
	v_cvt_pk_bf16_f32 v89, v250, v251
	v_cvt_pk_bf16_f32 v54, v208, v210
	v_lshlrev_b32_e32 v248, 16, v54
	v_and_b32_e32 v249, 0xffff0000, v54
	v_sub_f32_e32 v248, v208, v248
	v_sub_f32_e32 v249, v210, v249
	v_cvt_pk_bf16_f32 v58, v248, v249
	v_cvt_pk_bf16_f32 v55, v212, v214
	v_lshlrev_b32_e32 v250, 16, v55
	v_and_b32_e32 v251, 0xffff0000, v55
	v_sub_f32_e32 v250, v212, v250
	v_sub_f32_e32 v251, v214, v251
	v_cvt_pk_bf16_f32 v59, v250, v251
	v_cvt_pk_bf16_f32 v56, v216, v218
	v_lshlrev_b32_e32 v248, 16, v56
	v_and_b32_e32 v249, 0xffff0000, v56
	v_sub_f32_e32 v248, v216, v248
	v_sub_f32_e32 v249, v218, v249
	v_cvt_pk_bf16_f32 v60, v248, v249
	v_cvt_pk_bf16_f32 v57, v220, v222
	v_lshlrev_b32_e32 v250, 16, v57
	v_and_b32_e32 v251, 0xffff0000, v57
	v_sub_f32_e32 v250, v220, v250
	v_sub_f32_e32 v251, v222, v251
	v_cvt_pk_bf16_f32 v61, v250, v251
	v_cvt_pk_bf16_f32 v26, v209, v211
	v_lshlrev_b32_e32 v248, 16, v26
	v_and_b32_e32 v249, 0xffff0000, v26
	v_sub_f32_e32 v248, v209, v248
	v_sub_f32_e32 v249, v211, v249
	v_cvt_pk_bf16_f32 v22, v248, v249
	v_cvt_pk_bf16_f32 v27, v213, v215
	v_lshlrev_b32_e32 v250, 16, v27
	v_and_b32_e32 v251, 0xffff0000, v27
	v_sub_f32_e32 v250, v213, v250
	v_sub_f32_e32 v251, v215, v251
	v_cvt_pk_bf16_f32 v23, v250, v251
	v_cvt_pk_bf16_f32 v28, v217, v219
	v_lshlrev_b32_e32 v248, 16, v28
	v_and_b32_e32 v249, 0xffff0000, v28
	v_sub_f32_e32 v248, v217, v248
	v_sub_f32_e32 v249, v219, v249
	v_cvt_pk_bf16_f32 v24, v248, v249
	v_cvt_pk_bf16_f32 v29, v221, v223
	v_lshlrev_b32_e32 v250, 16, v29
	v_and_b32_e32 v251, 0xffff0000, v29
	v_sub_f32_e32 v250, v221, v250
	v_sub_f32_e32 v251, v223, v251
	v_cvt_pk_bf16_f32 v25, v250, v251
	v_cvt_pk_bf16_f32 v82, v136, v137
	v_lshlrev_b32_e32 v248, 16, v82
	v_and_b32_e32 v249, 0xffff0000, v82
	v_sub_f32_e32 v248, v136, v248
	v_sub_f32_e32 v249, v137, v249
	v_cvt_pk_bf16_f32 v78, v248, v249
	v_cvt_pk_bf16_f32 v83, v138, v139
	v_lshlrev_b32_e32 v250, 16, v83
	v_and_b32_e32 v251, 0xffff0000, v83
	v_sub_f32_e32 v250, v138, v250
	v_sub_f32_e32 v251, v139, v251
	v_cvt_pk_bf16_f32 v79, v250, v251
	v_cvt_pk_bf16_f32 v84, v140, v141
	v_lshlrev_b32_e32 v248, 16, v84
	v_and_b32_e32 v249, 0xffff0000, v84
	v_sub_f32_e32 v248, v140, v248
	v_sub_f32_e32 v249, v141, v249
	v_cvt_pk_bf16_f32 v80, v248, v249
	v_cvt_pk_bf16_f32 v85, v142, v143
	v_lshlrev_b32_e32 v250, 16, v85
	v_and_b32_e32 v251, 0xffff0000, v85
	v_sub_f32_e32 v250, v142, v250
	v_sub_f32_e32 v251, v143, v251
	v_cvt_pk_bf16_f32 v81, v250, v251
	v_cvt_pk_bf16_f32 v46, v224, v226
	v_lshlrev_b32_e32 v248, 16, v46
	v_and_b32_e32 v249, 0xffff0000, v46
	v_sub_f32_e32 v248, v224, v248
	v_sub_f32_e32 v249, v226, v249
	v_cvt_pk_bf16_f32 v50, v248, v249
	v_cvt_pk_bf16_f32 v47, v228, v230
	v_lshlrev_b32_e32 v250, 16, v47
	v_and_b32_e32 v251, 0xffff0000, v47
	v_sub_f32_e32 v250, v228, v250
	v_sub_f32_e32 v251, v230, v251
	v_cvt_pk_bf16_f32 v51, v250, v251
	v_cvt_pk_bf16_f32 v48, v232, v234
	v_lshlrev_b32_e32 v248, 16, v48
	v_and_b32_e32 v249, 0xffff0000, v48
	v_sub_f32_e32 v248, v232, v248
	v_sub_f32_e32 v249, v234, v249
	v_cvt_pk_bf16_f32 v52, v248, v249
	v_cvt_pk_bf16_f32 v49, v236, v238
	v_lshlrev_b32_e32 v250, 16, v49
	v_and_b32_e32 v251, 0xffff0000, v49
	v_sub_f32_e32 v250, v236, v250
	v_sub_f32_e32 v251, v238, v251
	v_cvt_pk_bf16_f32 v53, v250, v251
	v_cvt_pk_bf16_f32 v18, v225, v227
	v_lshlrev_b32_e32 v248, 16, v18
	v_and_b32_e32 v249, 0xffff0000, v18
	v_sub_f32_e32 v248, v225, v248
	v_sub_f32_e32 v249, v227, v249
	v_cvt_pk_bf16_f32 v14, v248, v249
	v_cvt_pk_bf16_f32 v19, v229, v231
	v_lshlrev_b32_e32 v250, 16, v19
	v_and_b32_e32 v251, 0xffff0000, v19
	v_sub_f32_e32 v250, v229, v250
	v_sub_f32_e32 v251, v231, v251
	v_cvt_pk_bf16_f32 v15, v250, v251
	v_cvt_pk_bf16_f32 v20, v233, v235
	v_lshlrev_b32_e32 v248, 16, v20
	v_and_b32_e32 v249, 0xffff0000, v20
	v_sub_f32_e32 v248, v233, v248
	v_sub_f32_e32 v249, v235, v249
	v_cvt_pk_bf16_f32 v16, v248, v249
	v_cvt_pk_bf16_f32 v21, v237, v239
	v_lshlrev_b32_e32 v250, 16, v21
	v_and_b32_e32 v251, 0xffff0000, v21
	v_sub_f32_e32 v250, v237, v250
	v_sub_f32_e32 v251, v239, v251
	v_cvt_pk_bf16_f32 v17, v250, v251
	v_mov_b32_e32 v113, 0
	v_cmp_gt_u32_e32 vcc, 0x100, v0
	v_and_b32_e32 v115, 63, v0
	v_lshrrev_b32_e32 v125, 2, v115
	v_lshlrev_b32_e32 v114, 2, v0
	v_and_b32_e32 v114, 12, v114
	v_mul_u32_u24_e32 v115, 20, v125
	v_mul_u32_u24_e32 v112, 0xa00, v149
	v_lshlrev_b32_e32 v115, 2, v115
	v_lshlrev_b32_e32 v120, 2, v114
	v_add3_u32 v118, v112, v115, v120
	v_lshlrev_b32_e32 v112, 2, v151
	v_lshl_add_u64 v[114:115], s[26:27], 0, v[112:113]
	v_mov_b32_e32 v112, 0x100
	v_cndmask_b32_e64 v112, v112, 0, vcc
	v_lshl_add_u64 v[122:123], s[28:29], 0, v[112:113]
	v_lshlrev_b32_e32 v112, 1, v153
	v_mov_b32_e32 v121, v113
	v_lshl_add_u64 v[112:113], v[122:123], 0, v[112:113]
	v_lshl_add_u64 v[114:115], v[114:115], 0, v[120:121]
	v_lshl_add_u64 v[112:113], v[112:113], 0, v[120:121]
	v_mul_u32_u24_e32 v120, 0x50, v152
	v_or_b32_e32 v120, v120, v150
	v_and_b32_e32 v124, 48, v0
	s_movk_i32 s4, 0xa00
	v_lshlrev_b32_e32 v120, 2, v120
	v_add_u32_e32 v122, s15, v125
	v_mul_u32_u24_e32 v116, 0x110, v1
	v_mul_u32_u24_e32 v117, 0x110, v146
	v_or_b32_e32 v119, 0xc350, v125
	s_max_u32 s6, s10, 1
	v_mad_u32_u24 v120, v149, s4, v120
	v_mad_u32_u24 v121, v150, s17, v124
	v_add_u32_e32 v122, 0xffffd887, v122
	v_and_b32_e32 v249, 63, v0
	v_and_b32_e32 v244, 31, v249
	v_lshlrev_b32_e32 v244, 4, v244
	v_mov_b32_e32 v245, 0
	v_lshl_add_u64 v[114:115], s[26:27], 0, v[244:245]
	v_lshl_add_u64 v[112:113], s[28:29], 0, v[244:245]
	v_lshrrev_b32_e32 v250, 5, v249
	v_lshl_add_u32 v250, v149, 1, v250
	v_sub_u32_e32 v253, v250, v125
	v_add_u32_e32 v254, 0xc350, v250
	v_mul_u32_u24_e32 v248, 528, v250
	v_add_u32_e32 v248, v248, v244
	v_add_u32_e32 v248, 52224, v248
	v_mul_u32_u24_e32 v246, 2112, v152
	v_lshl_add_u32 v246, v149, 6, v246
	v_lshl_add_u32 v246, v150, 2, v246
	v_mov_b32_e32 v247, v246
	v_add_u32_e32 v246, 52224, v246
	v_mul_u32_u24_e32 v247, 2112, v152
	v_and_b32_e32 v242, 3, v149
	v_lshlrev_b32_e32 v242, 6, v242
	v_lshrrev_b32_e32 v243, 2, v149
	v_lshlrev_b32_e32 v243, 8, v243
	v_add3_u32 v247, v247, v242, v243
	v_lshl_add_u32 v247, v150, 2, v247
	v_add_u32_e32 v247, 60672, v247
	s_mov_b32 s73, 0
	v_mov_b32_e32 v242, v254
	v_mov_b32_e32 v243, 0
	v_lshlrev_b64 v[244:245], 9, v[242:243]
	v_lshl_add_u64 v[228:229], v[114:115], 0, v[244:245]
	v_lshl_add_u64 v[230:231], v[112:113], 0, v[244:245]
	s_branch .LBB0_9

.LBB0_13:
	ds_read_b128 v[176:179], v123
	ds_read_b128 v[192:195], v123 offset:13056
	ds_read_b128 v[180:183], v123 offset:64
	ds_read_b128 v[196:199], v123 offset:13120
	ds_read_b128 v[184:187], v123 offset:128
	ds_read_b128 v[200:203], v123 offset:13184
	ds_read_b128 v[188:191], v123 offset:192
	ds_read_b128 v[204:207], v123 offset:13248
	s_add_i32 s8, s8, -1
	s_waitcnt lgkmcnt(6)
	v_mfma_f32_16x16x32_bf16 v[208:211], v[176:179], v[106:109], 0
	v_mfma_f32_16x16x32_bf16 v[212:215], v[176:179], v[74:77], 0
	v_mfma_f32_16x16x32_bf16 v[216:219], v[176:179], v[38:41], 0
	v_mfma_f32_16x16x32_bf16 v[208:211], v[192:195], v[106:109], v[208:211]
	v_mfma_f32_16x16x32_bf16 v[212:215], v[192:195], v[74:77], v[212:215]
	v_mfma_f32_16x16x32_bf16 v[216:219], v[192:195], v[38:41], v[216:219]
	v_mfma_f32_16x16x32_bf16 v[208:211], v[176:179], v[102:105], v[208:211]
	v_mfma_f32_16x16x32_bf16 v[212:215], v[176:179], v[70:73], v[212:215]
	v_mfma_f32_16x16x32_bf16 v[216:219], v[176:179], v[42:45], v[216:219]
	v_add_u32_e32 v240, s73, v246
	v_add_u32_e32 v241, s73, v247
	v_add_u32_e32 v242, 1056, v240
	v_add_u32_e32 v243, 1056, v241
	ds_write2_b32 v240, v220, v221 offset1:132
	ds_write2_b32 v241, v224, v225 offset1:132
	ds_write2_b32 v242, v222, v223 offset1:132
	ds_write2_b32 v243, v226, v227 offset1:132
	v_add_u32_e32 v123, 0x1100, v123
	s_waitcnt lgkmcnt(8)
	v_mfma_f32_16x16x32_bf16 v[208:211], v[180:183], v[98:101], v[208:211]
	v_mfma_f32_16x16x32_bf16 v[212:215], v[180:183], v[62:65], v[212:215]
	v_mfma_f32_16x16x32_bf16 v[216:219], v[180:183], v[30:33], v[216:219]
	v_mfma_f32_16x16x32_bf16 v[208:211], v[196:199], v[98:101], v[208:211]
	v_mfma_f32_16x16x32_bf16 v[212:215], v[196:199], v[62:65], v[212:215]
	v_mfma_f32_16x16x32_bf16 v[216:219], v[196:199], v[30:33], v[216:219]
	v_mfma_f32_16x16x32_bf16 v[208:211], v[180:183], v[94:97], v[208:211]
	v_mfma_f32_16x16x32_bf16 v[212:215], v[180:183], v[66:69], v[212:215]
	v_mfma_f32_16x16x32_bf16 v[216:219], v[180:183], v[34:37], v[216:219]
	s_waitcnt lgkmcnt(0)
	s_barrier
	v_add_u32_e32 v244, s73, v248
	ds_read_b128 v[232:235], v244
	ds_read_b128 v[236:239], v244 offset:8448
	v_mfma_f32_16x16x32_bf16 v[208:211], v[184:187], v[90:93], v[208:211]
	v_mfma_f32_16x16x32_bf16 v[212:215], v[184:187], v[54:57], v[212:215]
	v_mfma_f32_16x16x32_bf16 v[216:219], v[184:187], v[26:29], v[216:219]
	v_mfma_f32_16x16x32_bf16 v[208:211], v[200:203], v[90:93], v[208:211]
	v_mfma_f32_16x16x32_bf16 v[212:215], v[200:203], v[54:57], v[212:215]
	v_mfma_f32_16x16x32_bf16 v[216:219], v[200:203], v[26:29], v[216:219]
	v_mfma_f32_16x16x32_bf16 v[208:211], v[184:187], v[86:89], v[208:211]
	v_mfma_f32_16x16x32_bf16 v[212:215], v[184:187], v[58:61], v[212:215]
	v_mfma_f32_16x16x32_bf16 v[216:219], v[184:187], v[22:25], v[216:219]
	v_mfma_f32_16x16x32_bf16 v[208:211], v[188:191], v[82:85], v[208:211]
	v_mfma_f32_16x16x32_bf16 v[212:215], v[188:191], v[46:49], v[212:215]
	v_mfma_f32_16x16x32_bf16 v[216:219], v[188:191], v[18:21], v[216:219]
	s_waitcnt lgkmcnt(0)
	global_store_dwordx4 v[228:229], v[232:235], off
	global_store_dwordx4 v[230:231], v[236:239], off
	v_mfma_f32_16x16x32_bf16 v[208:211], v[204:207], v[82:85], v[208:211]
	v_mfma_f32_16x16x32_bf16 v[212:215], v[204:207], v[46:49], v[212:215]
	v_mfma_f32_16x16x32_bf16 v[216:219], v[204:207], v[18:21], v[216:219]
	v_mfma_f32_16x16x32_bf16 v[208:211], v[188:191], v[78:81], v[208:211]
	v_mfma_f32_16x16x32_bf16 v[212:215], v[188:191], v[50:53], v[212:215]
	v_mfma_f32_16x16x32_bf16 v[216:219], v[188:191], v[14:17], v[216:219]
	v_add_u32_e32 v242, v124, v253
	s_xor_b32 s73, s73, 16896
	v_cmp_gt_i32_e32 vcc, s12, v242
	s_cmp_eq_u32 s8, 0
	s_nop 1
	v_cndmask_b32_e32 v242, v254, v242, vcc
	v_ashrrev_i32_e32 v243, 31, v242
	v_lshlrev_b64 v[244:245], 9, v[242:243]
	v_add_u32_e32 v124, 16, v124
	v_lshl_add_u64 v[228:229], v[114:115], 0, v[244:245]
	v_lshl_add_u64 v[230:231], v[112:113], 0, v[244:245]
	v_mov_b32_e32 v220, v208
	v_mov_b32_e32 v221, v209
	v_mov_b32_e32 v222, v210
	v_mov_b32_e32 v223, v211
	v_cvt_pk_f16_f32 v224, v212, v216
	v_cvt_pk_f16_f32 v225, v213, v217
	v_cvt_pk_f16_f32 v226, v214, v218
	v_cvt_pk_f16_f32 v227, v215, v219
	s_cbranch_scc0 .LBB0_13

.Lg_drain:
	v_add_u32_e32 v240, s73, v246
	v_add_u32_e32 v241, s73, v247
	v_add_u32_e32 v242, 1056, v240
	v_add_u32_e32 v243, 1056, v241
	ds_write2_b32 v240, v220, v221 offset1:132
	ds_write2_b32 v241, v224, v225 offset1:132
	ds_write2_b32 v242, v222, v223 offset1:132
	ds_write2_b32 v243, v226, v227 offset1:132
	s_waitcnt lgkmcnt(0)
	s_barrier
	v_add_u32_e32 v244, s73, v248
	ds_read_b128 v[232:235], v244
	ds_read_b128 v[236:239], v244 offset:8448
	s_waitcnt lgkmcnt(0)
	global_store_dwordx4 v[228:229], v[232:235], off
	global_store_dwordx4 v[230:231], v[236:239], off

	.amdhsa_kernel _Z9l1_kernelPKiS0_P15HIP_vector_typeIjLj2EEPiS4_PKfS6_S6_S6_PfP6__half
		.amdhsa_group_segment_fixed_size 86016
		.amdhsa_private_segment_fixed_size 0
		.amdhsa_kernarg_size 88
		.amdhsa_user_sgpr_count 2
		.amdhsa_user_sgpr_dispatch_ptr 0
		.amdhsa_user_sgpr_queue_ptr 0
		.amdhsa_user_sgpr_kernarg_segment_ptr 1
		.amdhsa_user_sgpr_dispatch_id 0
		.amdhsa_user_sgpr_kernarg_preload_length 0
		.amdhsa_user_sgpr_kernarg_preload_offset 0
		.amdhsa_user_sgpr_private_segment_size 0
		.amdhsa_uses_dynamic_stack 0
		.amdhsa_enable_private_segment 0
		.amdhsa_system_sgpr_workgroup_id_x 1
		.amdhsa_system_sgpr_workgroup_id_y 0
		.amdhsa_system_sgpr_workgroup_id_z 0
		.amdhsa_system_sgpr_workgroup_info 0
		.amdhsa_system_vgpr_workitem_id 0
		.amdhsa_next_free_vgpr 256
		.amdhsa_next_free_sgpr 96
		.amdhsa_accum_offset 256
		.amdhsa_reserve_vcc 1
		.amdhsa_float_round_mode_32 0
		.amdhsa_float_round_mode_16_64 0
		.amdhsa_float_denorm_mode_32 3
		.amdhsa_float_denorm_mode_16_64 3
		.amdhsa_dx10_clamp 1
		.amdhsa_ieee_mode 1
		.amdhsa_fp16_overflow 0
		.amdhsa_tg_split 0
		.amdhsa_exception_fp_ieee_invalid_op 0
		.amdhsa_exception_fp_denorm_src 0
		.amdhsa_exception_fp_ieee_div_zero 0
		.amdhsa_exception_fp_ieee_overflow 0
		.amdhsa_exception_fp_ieee_underflow 0
		.amdhsa_exception_fp_ieee_inexact 0
		.amdhsa_exception_int_div_zero 0
	.end_amdhsa_kernel

amdhsa.kernels:
  - .agpr_count:     0
    .args:
      - .actual_access:  read_only
        .address_space:  global
        .offset:         0
        .size:           8
        .value_kind:     global_buffer
      - .actual_access:  read_only
        .address_space:  global
        .offset:         8
        .size:           8
        .value_kind:     global_buffer
      - .actual_access:  write_only
        .address_space:  global
        .offset:         16
        .size:           8
        .value_kind:     global_buffer
      - .actual_access:  write_only
        .address_space:  global
        .offset:         24
        .size:           8
        .value_kind:     global_buffer
      - .actual_access:  write_only
        .address_space:  global
        .offset:         32
        .size:           8
        .value_kind:     global_buffer
      - .actual_access:  read_only
        .address_space:  global
        .offset:         40
        .size:           8
        .value_kind:     global_buffer
      - .actual_access:  read_only
        .address_space:  global
        .offset:         48
        .size:           8
        .value_kind:     global_buffer
      - .actual_access:  read_only
        .address_space:  global
        .offset:         56
        .size:           8
        .value_kind:     global_buffer
      - .actual_access:  read_only
        .address_space:  global
        .offset:         64
        .size:           8
        .value_kind:     global_buffer
      - .actual_access:  write_only
        .address_space:  global
        .offset:         72
        .size:           8
        .value_kind:     global_buffer
      - .actual_access:  write_only
        .address_space:  global
        .offset:         80
        .size:           8
        .value_kind:     global_buffer
    .group_segment_fixed_size: 86016
    .kernarg_segment_align: 8
    .kernarg_segment_size: 88
    .language:       OpenCL C
    .language_version:
      - 2
      - 0
    .max_flat_workgroup_size: 512
    .name:           _Z9l1_kernelPKiS0_P15HIP_vector_typeIjLj2EEPiS4_PKfS6_S6_S6_PfP6__half
    .private_segment_fixed_size: 0
    .sgpr_count:     76
    .sgpr_spill_count: 0
    .symbol:         _Z9l1_kernelPKiS0_P15HIP_vector_typeIjLj2EEPiS4_PKfS6_S6_S6_PfP6__half.kd
    .uniform_work_group_size: 1
    .uses_dynamic_stack: false
    .vgpr_count:     256
    .vgpr_spill_count: 0
    .wavefront_size: 64
  - .agpr_count:     0
    .args:
      - .actual_access:  read_only
        .address_space:  global
        .offset:         0
        .size:           8
        .value_kind:     global_buffer
      - .actual_access:  read_only
        .address_space:  global
        .offset:         8
        .size:           8
        .value_kind:     global_buffer
      - .address_space:  global
        .offset:         16
        .size:           8
        .value_kind:     global_buffer
      - .address_space:  global
        .offset:         24
        .size:           8
        .value_kind:     global_buffer
      - .actual_access:  read_only
        .address_space:  global
        .offset:         32
        .size:           8
        .value_kind:     global_buffer
      - .actual_access:  read_only
        .address_space:  global
        .offset:         40
        .size:           8
        .value_kind:     global_buffer
      - .actual_access:  write_only
        .address_space:  global
        .offset:         48
        .size:           8
        .value_kind:     global_buffer
      - .actual_access:  write_only
        .address_space:  global
        .offset:         56
        .size:           8
        .value_kind:     global_buffer
    .group_segment_fixed_size: 159792
    .kernarg_segment_align: 8
    .kernarg_segment_size: 64
    .language:       OpenCL C
    .language_version:
      - 2
      - 0
    .max_flat_workgroup_size: 1024
    .name:           _Z11edge_kernelPK15HIP_vector_typeIjLj2EEPKiPiPS_IiLj2EEPKfPK6__halfPfSD_
    .private_segment_fixed_size: 0
    .sgpr_count:     72
    .sgpr_spill_count: 0
    .symbol:         _Z11edge_kernelPK15HIP_vector_typeIjLj2EEPKiPiPS_IiLj2EEPKfPK6__halfPfSD_.kd
    .uniform_work_group_size: 1
    .uses_dynamic_stack: false
    .vgpr_count:     128
    .vgpr_spill_count: 0
    .wavefront_size: 64
